# p8 GEMM K-loop (in-proj, gates): post-MFMA barrier moved up by 2 MFMAs so the MFMA pipe stays fed across the barrier hand-off between the two wave halves
# baseline (speedup 1.0000x reference)
.LBB0_226:
	s_add_u32 s30, s26, 0xfffc0080
	s_addc_u32 s31, s27, -1
	s_and_b64 s[28:29], s[28:29], exec
	s_cselect_b32 s31, s21, s31
	s_cselect_b32 s30, s20, s30
	s_cselect_b32 s29, s23, s52
	s_cselect_b32 s28, s22, s49
	s_add_i32 s54, 0, 0x10000
	v_add_u32_e32 v2, s54, v163
	ds_read_b128 v[132:135], v2
	ds_read_b128 v[136:139], v2 offset:1024
	ds_read_b128 v[140:143], v2 offset:2048
	ds_read_b128 v[144:147], v2 offset:3072
	v_lshl_add_u64 v[160:161], s[26:27], 0, v[156:157]
	s_add_i32 m0, s36, 0xc000
	ds_read_b128 v[166:169], v164
	ds_read_b128 v[170:173], v164 offset:1024
	ds_read_b128 v[174:177], v164 offset:2048
	ds_read_b128 v[178:181], v164 offset:3072
	ds_read_b128 v[182:185], v164 offset:4096
	ds_read_b128 v[186:189], v164 offset:5120
	ds_read_b128 v[190:193], v164 offset:6144
	ds_read_b128 v[194:197], v164 offset:7168
	global_load_lds_dwordx4 v[160:161], off
	v_lshl_add_u64 v[160:161], s[26:27], 0, v[158:159]
	s_add_i32 m0, s36, 0xe000
	s_nop 0
	global_load_lds_dwordx4 v[160:161], off
	s_waitcnt lgkmcnt(8)
	s_barrier
	s_waitcnt lgkmcnt(0)
	s_setprio 1
	s_waitcnt lgkmcnt(0)
	v_mfma_f32_16x16x32_bf16 v[128:131], v[132:135], v[166:169], v[128:131]
	v_mfma_f32_16x16x32_bf16 v[124:127], v[140:143], v[166:169], v[124:127]
	v_mfma_f32_16x16x32_bf16 v[116:119], v[132:135], v[174:177], v[116:119]
	v_mfma_f32_16x16x32_bf16 v[108:111], v[140:143], v[174:177], v[108:111]
	v_mfma_f32_16x16x32_bf16 v[100:103], v[132:135], v[182:185], v[100:103]
	v_mfma_f32_16x16x32_bf16 v[92:95], v[140:143], v[182:185], v[92:95]
	v_mfma_f32_16x16x32_bf16 v[84:87], v[132:135], v[190:193], v[84:87]
	v_mfma_f32_16x16x32_bf16 v[76:79], v[140:143], v[190:193], v[76:79]
	v_mfma_f32_16x16x32_bf16 v[128:131], v[136:139], v[170:173], v[128:131]
	v_mfma_f32_16x16x32_bf16 v[124:127], v[144:147], v[170:173], v[124:127]
	v_mfma_f32_16x16x32_bf16 v[116:119], v[136:139], v[178:181], v[116:119]
	v_mfma_f32_16x16x32_bf16 v[108:111], v[144:147], v[178:181], v[108:111]
	v_mfma_f32_16x16x32_bf16 v[100:103], v[136:139], v[186:189], v[100:103]
	v_mfma_f32_16x16x32_bf16 v[92:95], v[144:147], v[186:189], v[92:95]
	s_barrier
	v_mfma_f32_16x16x32_bf16 v[84:87], v[136:139], v[194:197], v[84:87]
	v_mfma_f32_16x16x32_bf16 v[76:79], v[144:147], v[194:197], v[76:79]
	s_setprio 0
	s_add_i32 s56, 0, 0x14000
	s_add_i32 s54, s54, s35
	v_add_u32_e32 v2, s56, v163
	v_lshl_add_u64 v[160:161], s[28:29], 0, v[150:151]
	s_mov_b32 m0, s54
	ds_read_b128 v[198:201], v2
	ds_read_b128 v[202:205], v2 offset:1024
	ds_read_b128 v[206:209], v2 offset:2048
	ds_read_b128 v[210:213], v2 offset:3072
	global_load_lds_dwordx4 v[160:161], off
	v_lshl_add_u64 v[222:223], s[28:29], 0, v[154:155]
	s_add_i32 m0, s54, 0x2000
	s_nop 0
	global_load_lds_dwordx4 v[222:223], off
	s_barrier
	s_waitcnt lgkmcnt(0)
	s_setprio 1
	s_waitcnt lgkmcnt(0)
	v_mfma_f32_16x16x32_bf16 v[120:123], v[198:201], v[166:169], v[120:123]
	v_mfma_f32_16x16x32_bf16 v[112:115], v[206:209], v[166:169], v[112:115]
	v_mfma_f32_16x16x32_bf16 v[104:107], v[198:201], v[174:177], v[104:107]
	v_mfma_f32_16x16x32_bf16 v[96:99], v[206:209], v[174:177], v[96:99]
	v_mfma_f32_16x16x32_bf16 v[88:91], v[198:201], v[182:185], v[88:91]
	v_mfma_f32_16x16x32_bf16 v[80:83], v[206:209], v[182:185], v[80:83]
	v_mfma_f32_16x16x32_bf16 v[72:75], v[198:201], v[190:193], v[72:75]
	v_mfma_f32_16x16x32_bf16 v[68:71], v[206:209], v[190:193], v[68:71]
	v_mfma_f32_16x16x32_bf16 v[120:123], v[202:205], v[170:173], v[120:123]
	v_mfma_f32_16x16x32_bf16 v[112:115], v[210:213], v[170:173], v[112:115]
	v_mfma_f32_16x16x32_bf16 v[104:107], v[202:205], v[178:181], v[104:107]
	v_mfma_f32_16x16x32_bf16 v[96:99], v[210:213], v[178:181], v[96:99]
	v_mfma_f32_16x16x32_bf16 v[88:91], v[202:205], v[186:189], v[88:91]
	v_mfma_f32_16x16x32_bf16 v[80:83], v[210:213], v[186:189], v[80:83]
	s_barrier
	v_mfma_f32_16x16x32_bf16 v[72:75], v[202:205], v[194:197], v[72:75]
	v_mfma_f32_16x16x32_bf16 v[68:71], v[210:213], v[194:197], v[68:71]
	s_setprio 0
	s_mov_b32 m0, s36
	v_lshl_add_u64 v[224:225], s[30:31], 0, v[148:149]
	ds_read_b128 v[166:169], v164 offset:16384
	ds_read_b128 v[170:173], v164 offset:17408
	ds_read_b128 v[174:177], v164 offset:18432
	ds_read_b128 v[178:181], v164 offset:19456
	ds_read_b128 v[182:185], v164 offset:20480
	ds_read_b128 v[186:189], v164 offset:21504
	ds_read_b128 v[190:193], v164 offset:22528
	ds_read_b128 v[194:197], v164 offset:23552
	global_load_lds_dwordx4 v[224:225], off
	v_lshl_add_u64 v[230:231], s[30:31], 0, v[152:153]
	s_mov_b32 m0, s37
	s_nop 0
	global_load_lds_dwordx4 v[230:231], off
	s_barrier
	s_waitcnt lgkmcnt(0)
	s_setprio 1
	s_waitcnt lgkmcnt(0)
	v_mfma_f32_16x16x32_bf16 v[64:67], v[132:135], v[166:169], v[64:67]
	v_mfma_f32_16x16x32_bf16 v[60:63], v[140:143], v[166:169], v[60:63]
	v_mfma_f32_16x16x32_bf16 v[52:55], v[132:135], v[174:177], v[52:55]
	v_mfma_f32_16x16x32_bf16 v[44:47], v[140:143], v[174:177], v[44:47]
	v_mfma_f32_16x16x32_bf16 v[36:39], v[132:135], v[182:185], v[36:39]
	v_mfma_f32_16x16x32_bf16 v[28:31], v[140:143], v[182:185], v[28:31]
	v_mfma_f32_16x16x32_bf16 v[20:23], v[132:135], v[190:193], v[20:23]
	v_mfma_f32_16x16x32_bf16 v[12:15], v[140:143], v[190:193], v[12:15]
	v_mfma_f32_16x16x32_bf16 v[64:67], v[136:139], v[170:173], v[64:67]
	v_mfma_f32_16x16x32_bf16 v[60:63], v[144:147], v[170:173], v[60:63]
	v_mfma_f32_16x16x32_bf16 v[52:55], v[136:139], v[178:181], v[52:55]
	v_mfma_f32_16x16x32_bf16 v[44:47], v[144:147], v[178:181], v[44:47]
	v_mfma_f32_16x16x32_bf16 v[36:39], v[136:139], v[186:189], v[36:39]
	v_mfma_f32_16x16x32_bf16 v[28:31], v[144:147], v[186:189], v[28:31]
	s_barrier
	v_mfma_f32_16x16x32_bf16 v[20:23], v[136:139], v[194:197], v[20:23]
	v_mfma_f32_16x16x32_bf16 v[12:15], v[144:147], v[194:197], v[12:15]
	s_setprio 0
	s_add_u32 s54, s28, 0x40000
	s_addc_u32 s55, s29, 0
	s_add_i32 s56, s56, s35
	v_lshl_add_u64 v[132:133], s[54:55], 0, v[150:151]
	s_mov_b32 m0, s56
	s_nop 0
	global_load_lds_dwordx4 v[132:133], off
	v_lshl_add_u64 v[132:133], s[54:55], 0, v[154:155]
	s_add_i32 m0, s56, 0x2000
	s_nop 0
	global_load_lds_dwordx4 v[132:133], off
	s_waitcnt vmcnt(6)
	s_barrier
	s_setprio 1
	v_mfma_f32_16x16x32_bf16 v[56:59], v[198:201], v[166:169], v[56:59]
	v_mfma_f32_16x16x32_bf16 v[48:51], v[206:209], v[166:169], v[48:51]
	v_mfma_f32_16x16x32_bf16 v[40:43], v[198:201], v[174:177], v[40:43]
	v_mfma_f32_16x16x32_bf16 v[32:35], v[206:209], v[174:177], v[32:35]
	v_mfma_f32_16x16x32_bf16 v[24:27], v[198:201], v[182:185], v[24:27]
	v_mfma_f32_16x16x32_bf16 v[16:19], v[206:209], v[182:185], v[16:19]
	v_mfma_f32_16x16x32_bf16 v[8:11], v[198:201], v[190:193], v[8:11]
	v_mfma_f32_16x16x32_bf16 v[4:7], v[206:209], v[190:193], v[4:7]
	v_mfma_f32_16x16x32_bf16 v[56:59], v[202:205], v[170:173], v[56:59]
	v_mfma_f32_16x16x32_bf16 v[48:51], v[210:213], v[170:173], v[48:51]
	v_mfma_f32_16x16x32_bf16 v[40:43], v[202:205], v[178:181], v[40:43]
	v_mfma_f32_16x16x32_bf16 v[32:35], v[210:213], v[178:181], v[32:35]
	v_mfma_f32_16x16x32_bf16 v[24:27], v[202:205], v[186:189], v[24:27]
	v_mfma_f32_16x16x32_bf16 v[16:19], v[210:213], v[186:189], v[16:19]
	s_barrier
	v_mfma_f32_16x16x32_bf16 v[8:11], v[202:205], v[194:197], v[8:11]
	v_mfma_f32_16x16x32_bf16 v[4:7], v[210:213], v[194:197], v[4:7]
	s_setprio 0
	s_add_i32 s54, 0, 0x18000
	v_add_u32_e32 v2, s54, v163
	ds_read_b128 v[132:135], v2
	ds_read_b128 v[136:139], v2 offset:1024
	ds_read_b128 v[140:143], v2 offset:2048
	ds_read_b128 v[144:147], v2 offset:3072
	s_add_u32 s30, s30, 0x40000
	s_addc_u32 s31, s31, 0
	s_mov_b32 m0, s38
	v_lshl_add_u64 v[198:199], s[30:31], 0, v[148:149]
	ds_read_b128 v[166:169], v164 offset:32768
	ds_read_b128 v[170:173], v164 offset:33792
	ds_read_b128 v[174:177], v164 offset:34816
	ds_read_b128 v[178:181], v164 offset:35840
	ds_read_b128 v[182:185], v164 offset:36864
	ds_read_b128 v[186:189], v164 offset:37888
	ds_read_b128 v[190:193], v164 offset:38912
	ds_read_b128 v[194:197], v164 offset:39936
	global_load_lds_dwordx4 v[198:199], off
	v_lshl_add_u64 v[198:199], s[30:31], 0, v[152:153]
	s_mov_b32 m0, s39
	s_nop 0
	global_load_lds_dwordx4 v[198:199], off
	s_waitcnt lgkmcnt(8)
	s_barrier
	s_waitcnt lgkmcnt(0)
	s_setprio 1
	s_waitcnt lgkmcnt(0)
	v_mfma_f32_16x16x32_bf16 v[128:131], v[132:135], v[166:169], v[128:131]
	v_mfma_f32_16x16x32_bf16 v[124:127], v[140:143], v[166:169], v[124:127]
	v_mfma_f32_16x16x32_bf16 v[116:119], v[132:135], v[174:177], v[116:119]
	v_mfma_f32_16x16x32_bf16 v[108:111], v[140:143], v[174:177], v[108:111]
	v_mfma_f32_16x16x32_bf16 v[100:103], v[132:135], v[182:185], v[100:103]
	v_mfma_f32_16x16x32_bf16 v[92:95], v[140:143], v[182:185], v[92:95]
	v_mfma_f32_16x16x32_bf16 v[84:87], v[132:135], v[190:193], v[84:87]
	v_mfma_f32_16x16x32_bf16 v[76:79], v[140:143], v[190:193], v[76:79]
	v_mfma_f32_16x16x32_bf16 v[128:131], v[136:139], v[170:173], v[128:131]
	v_mfma_f32_16x16x32_bf16 v[124:127], v[144:147], v[170:173], v[124:127]
	v_mfma_f32_16x16x32_bf16 v[116:119], v[136:139], v[178:181], v[116:119]
	v_mfma_f32_16x16x32_bf16 v[108:111], v[144:147], v[178:181], v[108:111]
	v_mfma_f32_16x16x32_bf16 v[100:103], v[136:139], v[186:189], v[100:103]
	v_mfma_f32_16x16x32_bf16 v[92:95], v[144:147], v[186:189], v[92:95]
	s_barrier
	v_mfma_f32_16x16x32_bf16 v[84:87], v[136:139], v[194:197], v[84:87]
	v_mfma_f32_16x16x32_bf16 v[76:79], v[144:147], v[194:197], v[76:79]
	s_setprio 0
	s_add_i32 s30, 0, 0x1c000
	s_add_i32 s31, s54, s35
	v_add_u32_e32 v2, s30, v163
	v_lshl_add_u64 v[160:161], v[160:161], 0, s[60:61]
	s_mov_b32 m0, s31
	ds_read_b128 v[198:201], v2
	ds_read_b128 v[202:205], v2 offset:1024
	ds_read_b128 v[206:209], v2 offset:2048
	ds_read_b128 v[210:213], v2 offset:3072
	global_load_lds_dwordx4 v[160:161], off
	v_lshl_add_u64 v[160:161], v[222:223], 0, s[60:61]
	s_add_i32 m0, s31, 0x2000
	s_nop 0
	global_load_lds_dwordx4 v[160:161], off
	s_barrier
	s_waitcnt lgkmcnt(0)
	s_setprio 1
	s_waitcnt lgkmcnt(0)
	v_mfma_f32_16x16x32_bf16 v[120:123], v[198:201], v[166:169], v[120:123]
	v_mfma_f32_16x16x32_bf16 v[112:115], v[206:209], v[166:169], v[112:115]
	v_mfma_f32_16x16x32_bf16 v[104:107], v[198:201], v[174:177], v[104:107]
	v_mfma_f32_16x16x32_bf16 v[96:99], v[206:209], v[174:177], v[96:99]
	v_mfma_f32_16x16x32_bf16 v[88:91], v[198:201], v[182:185], v[88:91]
	v_mfma_f32_16x16x32_bf16 v[80:83], v[206:209], v[182:185], v[80:83]
	v_mfma_f32_16x16x32_bf16 v[72:75], v[198:201], v[190:193], v[72:75]
	v_mfma_f32_16x16x32_bf16 v[68:71], v[206:209], v[190:193], v[68:71]
	v_mfma_f32_16x16x32_bf16 v[120:123], v[202:205], v[170:173], v[120:123]
	v_mfma_f32_16x16x32_bf16 v[112:115], v[210:213], v[170:173], v[112:115]
	v_mfma_f32_16x16x32_bf16 v[104:107], v[202:205], v[178:181], v[104:107]
	v_mfma_f32_16x16x32_bf16 v[96:99], v[210:213], v[178:181], v[96:99]
	v_mfma_f32_16x16x32_bf16 v[88:91], v[202:205], v[186:189], v[88:91]
	v_mfma_f32_16x16x32_bf16 v[80:83], v[210:213], v[186:189], v[80:83]
	s_barrier
	v_mfma_f32_16x16x32_bf16 v[72:75], v[202:205], v[194:197], v[72:75]
	v_mfma_f32_16x16x32_bf16 v[68:71], v[210:213], v[194:197], v[68:71]
	s_setprio 0
	s_mov_b32 m0, s42
	v_lshl_add_u64 v[160:161], v[224:225], 0, s[60:61]
	ds_read_b128 v[166:169], v164 offset:49152
	ds_read_b128 v[170:173], v164 offset:50176
	ds_read_b128 v[174:177], v164 offset:51200
	ds_read_b128 v[178:181], v164 offset:52224
	ds_read_b128 v[182:185], v164 offset:53248
	ds_read_b128 v[186:189], v164 offset:54272
	ds_read_b128 v[190:193], v164 offset:55296
	ds_read_b128 v[194:197], v164 offset:56320
	global_load_lds_dwordx4 v[160:161], off
	v_lshl_add_u64 v[160:161], v[230:231], 0, s[60:61]
	s_mov_b32 m0, s43
	s_nop 0
	global_load_lds_dwordx4 v[160:161], off
	s_barrier
	s_waitcnt lgkmcnt(0)
	s_setprio 1
	s_waitcnt lgkmcnt(0)
	v_mfma_f32_16x16x32_bf16 v[64:67], v[132:135], v[166:169], v[64:67]
	v_mfma_f32_16x16x32_bf16 v[60:63], v[140:143], v[166:169], v[60:63]
	v_mfma_f32_16x16x32_bf16 v[52:55], v[132:135], v[174:177], v[52:55]
	v_mfma_f32_16x16x32_bf16 v[44:47], v[140:143], v[174:177], v[44:47]
	v_mfma_f32_16x16x32_bf16 v[36:39], v[132:135], v[182:185], v[36:39]
	v_mfma_f32_16x16x32_bf16 v[28:31], v[140:143], v[182:185], v[28:31]
	v_mfma_f32_16x16x32_bf16 v[20:23], v[132:135], v[190:193], v[20:23]
	v_mfma_f32_16x16x32_bf16 v[12:15], v[140:143], v[190:193], v[12:15]
	v_mfma_f32_16x16x32_bf16 v[64:67], v[136:139], v[170:173], v[64:67]
	v_mfma_f32_16x16x32_bf16 v[60:63], v[144:147], v[170:173], v[60:63]
	v_mfma_f32_16x16x32_bf16 v[52:55], v[136:139], v[178:181], v[52:55]
	v_mfma_f32_16x16x32_bf16 v[44:47], v[144:147], v[178:181], v[44:47]
	v_mfma_f32_16x16x32_bf16 v[36:39], v[136:139], v[186:189], v[36:39]
	v_mfma_f32_16x16x32_bf16 v[28:31], v[144:147], v[186:189], v[28:31]
	s_barrier
	v_mfma_f32_16x16x32_bf16 v[20:23], v[136:139], v[194:197], v[20:23]
	v_mfma_f32_16x16x32_bf16 v[12:15], v[144:147], v[194:197], v[12:15]
	s_setprio 0
	s_add_u32 s28, s28, 0x40080
	s_addc_u32 s29, s29, 0
	s_add_i32 s30, s30, s35
	v_lshl_add_u64 v[132:133], s[28:29], 0, v[150:151]
	s_mov_b32 m0, s30
	s_nop 0
	global_load_lds_dwordx4 v[132:133], off
	v_lshl_add_u64 v[132:133], s[28:29], 0, v[154:155]
	s_add_i32 m0, s30, 0x2000
	s_nop 0
	global_load_lds_dwordx4 v[132:133], off
	s_waitcnt vmcnt(6)
	s_barrier
	s_setprio 1
	v_mfma_f32_16x16x32_bf16 v[56:59], v[198:201], v[166:169], v[56:59]
	v_mfma_f32_16x16x32_bf16 v[48:51], v[206:209], v[166:169], v[48:51]
	v_mfma_f32_16x16x32_bf16 v[40:43], v[198:201], v[174:177], v[40:43]
	v_mfma_f32_16x16x32_bf16 v[32:35], v[206:209], v[174:177], v[32:35]
	v_mfma_f32_16x16x32_bf16 v[24:27], v[198:201], v[182:185], v[24:27]
	v_mfma_f32_16x16x32_bf16 v[16:19], v[206:209], v[182:185], v[16:19]
	v_mfma_f32_16x16x32_bf16 v[8:11], v[198:201], v[190:193], v[8:11]
	v_mfma_f32_16x16x32_bf16 v[4:7], v[206:209], v[190:193], v[4:7]
	v_mfma_f32_16x16x32_bf16 v[56:59], v[202:205], v[170:173], v[56:59]
	v_mfma_f32_16x16x32_bf16 v[48:51], v[210:213], v[170:173], v[48:51]
	v_mfma_f32_16x16x32_bf16 v[40:43], v[202:205], v[178:181], v[40:43]
	v_mfma_f32_16x16x32_bf16 v[32:35], v[210:213], v[178:181], v[32:35]
	v_mfma_f32_16x16x32_bf16 v[24:27], v[202:205], v[186:189], v[24:27]
	v_mfma_f32_16x16x32_bf16 v[16:19], v[210:213], v[186:189], v[16:19]
	s_barrier
	v_mfma_f32_16x16x32_bf16 v[8:11], v[202:205], v[194:197], v[8:11]
	v_mfma_f32_16x16x32_bf16 v[4:7], v[210:213], v[194:197], v[4:7]
	s_setprio 0
	s_add_i32 s53, s53, 2
	s_add_u32 s26, s26, 0x100
	s_addc_u32 s27, s27, 0
	s_add_u32 s49, s49, 0x100
	s_addc_u32 s52, s52, 0
	s_cmp_gt_u32 s53, 13
	s_cbranch_scc1 .LBB0_230

.Lmy_bias_skip:
	s_add_u32 s38, s34, 0xfffc0080
	s_addc_u32 s39, s35, -1
	s_and_b64 s[36:37], s[36:37], exec
	s_cselect_b32 s39, s27, s39
	s_cselect_b32 s38, s26, s38
	s_cselect_b32 s37, s29, s63
	s_cselect_b32 s36, s28, s62
	s_add_i32 s65, 0, 0x10000
	v_add_u32_e32 v2, s65, v163
	ds_read_b128 v[132:135], v2
	ds_read_b128 v[136:139], v2 offset:1024
	ds_read_b128 v[140:143], v2 offset:2048
	ds_read_b128 v[144:147], v2 offset:3072
	v_lshl_add_u64 v[160:161], s[34:35], 0, v[156:157]
	s_add_i32 m0, s42, 0xc000
	ds_read_b128 v[166:169], v164
	ds_read_b128 v[170:173], v164 offset:1024
	ds_read_b128 v[174:177], v164 offset:2048
	ds_read_b128 v[178:181], v164 offset:3072
	ds_read_b128 v[182:185], v164 offset:4096
	ds_read_b128 v[186:189], v164 offset:5120
	ds_read_b128 v[190:193], v164 offset:6144
	ds_read_b128 v[194:197], v164 offset:7168
	global_load_lds_dwordx4 v[160:161], off
	v_lshl_add_u64 v[160:161], s[34:35], 0, v[158:159]
	s_add_i32 m0, s42, 0xe000
	s_nop 0
	global_load_lds_dwordx4 v[160:161], off
	s_waitcnt lgkmcnt(8)
	s_barrier
	s_waitcnt lgkmcnt(0)
	s_setprio 1
	s_waitcnt lgkmcnt(0)
	v_mfma_f32_16x16x32_bf16 v[128:131], v[132:135], v[166:169], v[128:131]
	v_mfma_f32_16x16x32_bf16 v[124:127], v[140:143], v[166:169], v[124:127]
	v_mfma_f32_16x16x32_bf16 v[112:115], v[132:135], v[174:177], v[112:115]
	v_mfma_f32_16x16x32_bf16 v[108:111], v[140:143], v[174:177], v[108:111]
	v_mfma_f32_16x16x32_bf16 v[96:99], v[132:135], v[182:185], v[96:99]
	v_mfma_f32_16x16x32_bf16 v[92:95], v[140:143], v[182:185], v[92:95]
	v_mfma_f32_16x16x32_bf16 v[80:83], v[132:135], v[190:193], v[80:83]
	v_mfma_f32_16x16x32_bf16 v[76:79], v[140:143], v[190:193], v[76:79]
	v_mfma_f32_16x16x32_bf16 v[128:131], v[136:139], v[170:173], v[128:131]
	v_mfma_f32_16x16x32_bf16 v[124:127], v[144:147], v[170:173], v[124:127]
	v_mfma_f32_16x16x32_bf16 v[112:115], v[136:139], v[178:181], v[112:115]
	v_mfma_f32_16x16x32_bf16 v[108:111], v[144:147], v[178:181], v[108:111]
	v_mfma_f32_16x16x32_bf16 v[96:99], v[136:139], v[186:189], v[96:99]
	v_mfma_f32_16x16x32_bf16 v[92:95], v[144:147], v[186:189], v[92:95]
	s_barrier
	v_mfma_f32_16x16x32_bf16 v[80:83], v[136:139], v[194:197], v[80:83]
	v_mfma_f32_16x16x32_bf16 v[76:79], v[144:147], v[194:197], v[76:79]
	s_setprio 0
	s_add_i32 s68, 0, 0x14000
	s_add_i32 s65, s65, s41
	v_add_u32_e32 v2, s68, v163
	v_lshl_add_u64 v[160:161], s[36:37], 0, v[150:151]
	s_mov_b32 m0, s65
	ds_read_b128 v[198:201], v2
	ds_read_b128 v[202:205], v2 offset:1024
	ds_read_b128 v[206:209], v2 offset:2048
	ds_read_b128 v[210:213], v2 offset:3072
	global_load_lds_dwordx4 v[160:161], off
	v_lshl_add_u64 v[222:223], s[36:37], 0, v[154:155]
	s_add_i32 m0, s65, 0x2000
	s_nop 0
	global_load_lds_dwordx4 v[222:223], off
	s_barrier
	s_waitcnt lgkmcnt(0)
	s_setprio 1
	s_waitcnt lgkmcnt(0)
	v_mfma_f32_16x16x32_bf16 v[120:123], v[198:201], v[166:169], v[120:123]
	v_mfma_f32_16x16x32_bf16 v[116:119], v[206:209], v[166:169], v[116:119]
	v_mfma_f32_16x16x32_bf16 v[104:107], v[198:201], v[174:177], v[104:107]
	v_mfma_f32_16x16x32_bf16 v[100:103], v[206:209], v[174:177], v[100:103]
	v_mfma_f32_16x16x32_bf16 v[88:91], v[198:201], v[182:185], v[88:91]
	v_mfma_f32_16x16x32_bf16 v[84:87], v[206:209], v[182:185], v[84:87]
	v_mfma_f32_16x16x32_bf16 v[72:75], v[198:201], v[190:193], v[72:75]
	v_mfma_f32_16x16x32_bf16 v[68:71], v[206:209], v[190:193], v[68:71]
	v_mfma_f32_16x16x32_bf16 v[120:123], v[202:205], v[170:173], v[120:123]
	v_mfma_f32_16x16x32_bf16 v[116:119], v[210:213], v[170:173], v[116:119]
	v_mfma_f32_16x16x32_bf16 v[104:107], v[202:205], v[178:181], v[104:107]
	v_mfma_f32_16x16x32_bf16 v[100:103], v[210:213], v[178:181], v[100:103]
	v_mfma_f32_16x16x32_bf16 v[88:91], v[202:205], v[186:189], v[88:91]
	v_mfma_f32_16x16x32_bf16 v[84:87], v[210:213], v[186:189], v[84:87]
	s_barrier
	v_mfma_f32_16x16x32_bf16 v[72:75], v[202:205], v[194:197], v[72:75]
	v_mfma_f32_16x16x32_bf16 v[68:71], v[210:213], v[194:197], v[68:71]
	s_setprio 0
	s_mov_b32 m0, s42
	v_lshl_add_u64 v[224:225], s[38:39], 0, v[148:149]
	ds_read_b128 v[166:169], v164 offset:16384
	ds_read_b128 v[170:173], v164 offset:17408
	ds_read_b128 v[174:177], v164 offset:18432
	ds_read_b128 v[178:181], v164 offset:19456
	ds_read_b128 v[182:185], v164 offset:20480
	ds_read_b128 v[186:189], v164 offset:21504
	ds_read_b128 v[190:193], v164 offset:22528
	ds_read_b128 v[194:197], v164 offset:23552
	global_load_lds_dwordx4 v[224:225], off
	v_lshl_add_u64 v[230:231], s[38:39], 0, v[152:153]
	s_mov_b32 m0, s43
	s_nop 0
	global_load_lds_dwordx4 v[230:231], off
	s_barrier
	s_waitcnt lgkmcnt(0)
	s_setprio 1
	s_waitcnt lgkmcnt(0)
	v_mfma_f32_16x16x32_bf16 v[64:67], v[132:135], v[166:169], v[64:67]
	v_mfma_f32_16x16x32_bf16 v[60:63], v[140:143], v[166:169], v[60:63]
	v_mfma_f32_16x16x32_bf16 v[48:51], v[132:135], v[174:177], v[48:51]
	v_mfma_f32_16x16x32_bf16 v[44:47], v[140:143], v[174:177], v[44:47]
	v_mfma_f32_16x16x32_bf16 v[32:35], v[132:135], v[182:185], v[32:35]
	v_mfma_f32_16x16x32_bf16 v[28:31], v[140:143], v[182:185], v[28:31]
	v_mfma_f32_16x16x32_bf16 v[16:19], v[132:135], v[190:193], v[16:19]
	v_mfma_f32_16x16x32_bf16 v[12:15], v[140:143], v[190:193], v[12:15]
	v_mfma_f32_16x16x32_bf16 v[64:67], v[136:139], v[170:173], v[64:67]
	v_mfma_f32_16x16x32_bf16 v[60:63], v[144:147], v[170:173], v[60:63]
	v_mfma_f32_16x16x32_bf16 v[48:51], v[136:139], v[178:181], v[48:51]
	v_mfma_f32_16x16x32_bf16 v[44:47], v[144:147], v[178:181], v[44:47]
	v_mfma_f32_16x16x32_bf16 v[32:35], v[136:139], v[186:189], v[32:35]
	v_mfma_f32_16x16x32_bf16 v[28:31], v[144:147], v[186:189], v[28:31]
	s_barrier
	v_mfma_f32_16x16x32_bf16 v[16:19], v[136:139], v[194:197], v[16:19]
	v_mfma_f32_16x16x32_bf16 v[12:15], v[144:147], v[194:197], v[12:15]
	s_setprio 0
	s_add_u32 s66, s36, 0x40000
	s_addc_u32 s67, s37, 0
	s_add_i32 s65, s68, s41
	v_lshl_add_u64 v[132:133], s[66:67], 0, v[150:151]
	s_mov_b32 m0, s65
	s_nop 0
	global_load_lds_dwordx4 v[132:133], off
	v_lshl_add_u64 v[132:133], s[66:67], 0, v[154:155]
	s_add_i32 m0, s65, 0x2000
	s_nop 0
	global_load_lds_dwordx4 v[132:133], off
	s_waitcnt vmcnt(6)
	s_barrier
	s_setprio 1
	v_mfma_f32_16x16x32_bf16 v[56:59], v[198:201], v[166:169], v[56:59]
	v_mfma_f32_16x16x32_bf16 v[52:55], v[206:209], v[166:169], v[52:55]
	v_mfma_f32_16x16x32_bf16 v[40:43], v[198:201], v[174:177], v[40:43]
	v_mfma_f32_16x16x32_bf16 v[36:39], v[206:209], v[174:177], v[36:39]
	v_mfma_f32_16x16x32_bf16 v[24:27], v[198:201], v[182:185], v[24:27]
	v_mfma_f32_16x16x32_bf16 v[20:23], v[206:209], v[182:185], v[20:23]
	v_mfma_f32_16x16x32_bf16 v[8:11], v[198:201], v[190:193], v[8:11]
	v_mfma_f32_16x16x32_bf16 v[4:7], v[206:209], v[190:193], v[4:7]
	v_mfma_f32_16x16x32_bf16 v[56:59], v[202:205], v[170:173], v[56:59]
	v_mfma_f32_16x16x32_bf16 v[52:55], v[210:213], v[170:173], v[52:55]
	v_mfma_f32_16x16x32_bf16 v[40:43], v[202:205], v[178:181], v[40:43]
	v_mfma_f32_16x16x32_bf16 v[36:39], v[210:213], v[178:181], v[36:39]
	v_mfma_f32_16x16x32_bf16 v[24:27], v[202:205], v[186:189], v[24:27]
	v_mfma_f32_16x16x32_bf16 v[20:23], v[210:213], v[186:189], v[20:23]
	s_barrier
	v_mfma_f32_16x16x32_bf16 v[8:11], v[202:205], v[194:197], v[8:11]
	v_mfma_f32_16x16x32_bf16 v[4:7], v[210:213], v[194:197], v[4:7]
	s_setprio 0
	s_add_i32 s65, 0, 0x18000
	v_add_u32_e32 v2, s65, v163
	ds_read_b128 v[132:135], v2
	ds_read_b128 v[136:139], v2 offset:1024
	ds_read_b128 v[140:143], v2 offset:2048
	ds_read_b128 v[144:147], v2 offset:3072
	s_add_u32 s38, s38, 0x40000
	s_addc_u32 s39, s39, 0
	s_mov_b32 m0, s44
	v_lshl_add_u64 v[198:199], s[38:39], 0, v[148:149]
	ds_read_b128 v[166:169], v164 offset:32768
	ds_read_b128 v[170:173], v164 offset:33792
	ds_read_b128 v[174:177], v164 offset:34816
	ds_read_b128 v[178:181], v164 offset:35840
	ds_read_b128 v[182:185], v164 offset:36864
	ds_read_b128 v[186:189], v164 offset:37888
	ds_read_b128 v[190:193], v164 offset:38912
	ds_read_b128 v[194:197], v164 offset:39936
	global_load_lds_dwordx4 v[198:199], off
	v_lshl_add_u64 v[198:199], s[38:39], 0, v[152:153]
	s_mov_b32 m0, s45
	s_nop 0
	global_load_lds_dwordx4 v[198:199], off
	s_waitcnt lgkmcnt(8)
	s_barrier
	s_waitcnt lgkmcnt(0)
	s_setprio 1
	s_waitcnt lgkmcnt(0)
	v_mfma_f32_16x16x32_bf16 v[128:131], v[132:135], v[166:169], v[128:131]
	v_mfma_f32_16x16x32_bf16 v[124:127], v[140:143], v[166:169], v[124:127]
	v_mfma_f32_16x16x32_bf16 v[112:115], v[132:135], v[174:177], v[112:115]
	v_mfma_f32_16x16x32_bf16 v[108:111], v[140:143], v[174:177], v[108:111]
	v_mfma_f32_16x16x32_bf16 v[96:99], v[132:135], v[182:185], v[96:99]
	v_mfma_f32_16x16x32_bf16 v[92:95], v[140:143], v[182:185], v[92:95]
	v_mfma_f32_16x16x32_bf16 v[80:83], v[132:135], v[190:193], v[80:83]
	v_mfma_f32_16x16x32_bf16 v[76:79], v[140:143], v[190:193], v[76:79]
	v_mfma_f32_16x16x32_bf16 v[128:131], v[136:139], v[170:173], v[128:131]
	v_mfma_f32_16x16x32_bf16 v[124:127], v[144:147], v[170:173], v[124:127]
	v_mfma_f32_16x16x32_bf16 v[112:115], v[136:139], v[178:181], v[112:115]
	v_mfma_f32_16x16x32_bf16 v[108:111], v[144:147], v[178:181], v[108:111]
	v_mfma_f32_16x16x32_bf16 v[96:99], v[136:139], v[186:189], v[96:99]
	v_mfma_f32_16x16x32_bf16 v[92:95], v[144:147], v[186:189], v[92:95]
	s_barrier
	v_mfma_f32_16x16x32_bf16 v[80:83], v[136:139], v[194:197], v[80:83]
	v_mfma_f32_16x16x32_bf16 v[76:79], v[144:147], v[194:197], v[76:79]
	s_setprio 0
	s_add_i32 s38, 0, 0x1c000
	s_add_i32 s39, s65, s41
	v_add_u32_e32 v2, s38, v163
	v_lshl_add_u64 v[160:161], v[160:161], 0, s[60:61]
	s_mov_b32 m0, s39
	ds_read_b128 v[198:201], v2
	ds_read_b128 v[202:205], v2 offset:1024
	ds_read_b128 v[206:209], v2 offset:2048
	ds_read_b128 v[210:213], v2 offset:3072
	global_load_lds_dwordx4 v[160:161], off
	v_lshl_add_u64 v[160:161], v[222:223], 0, s[60:61]
	s_add_i32 m0, s39, 0x2000
	s_nop 0
	global_load_lds_dwordx4 v[160:161], off
	s_barrier
	s_waitcnt lgkmcnt(0)
	s_setprio 1
	s_waitcnt lgkmcnt(0)
	v_mfma_f32_16x16x32_bf16 v[120:123], v[198:201], v[166:169], v[120:123]
	v_mfma_f32_16x16x32_bf16 v[116:119], v[206:209], v[166:169], v[116:119]
	v_mfma_f32_16x16x32_bf16 v[104:107], v[198:201], v[174:177], v[104:107]
	v_mfma_f32_16x16x32_bf16 v[100:103], v[206:209], v[174:177], v[100:103]
	v_mfma_f32_16x16x32_bf16 v[88:91], v[198:201], v[182:185], v[88:91]
	v_mfma_f32_16x16x32_bf16 v[84:87], v[206:209], v[182:185], v[84:87]
	v_mfma_f32_16x16x32_bf16 v[72:75], v[198:201], v[190:193], v[72:75]
	v_mfma_f32_16x16x32_bf16 v[68:71], v[206:209], v[190:193], v[68:71]
	v_mfma_f32_16x16x32_bf16 v[120:123], v[202:205], v[170:173], v[120:123]
	v_mfma_f32_16x16x32_bf16 v[116:119], v[210:213], v[170:173], v[116:119]
	v_mfma_f32_16x16x32_bf16 v[104:107], v[202:205], v[178:181], v[104:107]
	v_mfma_f32_16x16x32_bf16 v[100:103], v[210:213], v[178:181], v[100:103]
	v_mfma_f32_16x16x32_bf16 v[88:91], v[202:205], v[186:189], v[88:91]
	v_mfma_f32_16x16x32_bf16 v[84:87], v[210:213], v[186:189], v[84:87]
	s_barrier
	v_mfma_f32_16x16x32_bf16 v[72:75], v[202:205], v[194:197], v[72:75]
	v_mfma_f32_16x16x32_bf16 v[68:71], v[210:213], v[194:197], v[68:71]
	s_setprio 0
	s_mov_b32 m0, s48
	v_lshl_add_u64 v[160:161], v[224:225], 0, s[60:61]
	ds_read_b128 v[166:169], v164 offset:49152
	ds_read_b128 v[170:173], v164 offset:50176
	ds_read_b128 v[174:177], v164 offset:51200
	ds_read_b128 v[178:181], v164 offset:52224
	ds_read_b128 v[182:185], v164 offset:53248
	ds_read_b128 v[186:189], v164 offset:54272
	ds_read_b128 v[190:193], v164 offset:55296
	ds_read_b128 v[194:197], v164 offset:56320
	global_load_lds_dwordx4 v[160:161], off
	v_lshl_add_u64 v[160:161], v[230:231], 0, s[60:61]
	s_mov_b32 m0, s49
	s_nop 0
	global_load_lds_dwordx4 v[160:161], off
	s_barrier
	s_waitcnt lgkmcnt(0)
	s_setprio 1
	s_waitcnt lgkmcnt(0)
	v_mfma_f32_16x16x32_bf16 v[64:67], v[132:135], v[166:169], v[64:67]
	v_mfma_f32_16x16x32_bf16 v[60:63], v[140:143], v[166:169], v[60:63]
	v_mfma_f32_16x16x32_bf16 v[48:51], v[132:135], v[174:177], v[48:51]
	v_mfma_f32_16x16x32_bf16 v[44:47], v[140:143], v[174:177], v[44:47]
	v_mfma_f32_16x16x32_bf16 v[32:35], v[132:135], v[182:185], v[32:35]
	v_mfma_f32_16x16x32_bf16 v[28:31], v[140:143], v[182:185], v[28:31]
	v_mfma_f32_16x16x32_bf16 v[16:19], v[132:135], v[190:193], v[16:19]
	v_mfma_f32_16x16x32_bf16 v[12:15], v[140:143], v[190:193], v[12:15]
	v_mfma_f32_16x16x32_bf16 v[64:67], v[136:139], v[170:173], v[64:67]
	v_mfma_f32_16x16x32_bf16 v[60:63], v[144:147], v[170:173], v[60:63]
	v_mfma_f32_16x16x32_bf16 v[48:51], v[136:139], v[178:181], v[48:51]
	v_mfma_f32_16x16x32_bf16 v[44:47], v[144:147], v[178:181], v[44:47]
	v_mfma_f32_16x16x32_bf16 v[32:35], v[136:139], v[186:189], v[32:35]
	v_mfma_f32_16x16x32_bf16 v[28:31], v[144:147], v[186:189], v[28:31]
	s_barrier
	v_mfma_f32_16x16x32_bf16 v[16:19], v[136:139], v[194:197], v[16:19]
	v_mfma_f32_16x16x32_bf16 v[12:15], v[144:147], v[194:197], v[12:15]
	s_setprio 0
	s_add_u32 s36, s36, 0x40080
	s_addc_u32 s37, s37, 0
	s_add_i32 s38, s38, s41
	v_lshl_add_u64 v[132:133], s[36:37], 0, v[150:151]
	s_mov_b32 m0, s38
	s_nop 0
	global_load_lds_dwordx4 v[132:133], off
	v_lshl_add_u64 v[132:133], s[36:37], 0, v[154:155]
	s_add_i32 m0, s38, 0x2000
	s_nop 0
	global_load_lds_dwordx4 v[132:133], off
	s_waitcnt vmcnt(6)
	s_barrier
	s_setprio 1
	v_mfma_f32_16x16x32_bf16 v[56:59], v[198:201], v[166:169], v[56:59]
	v_mfma_f32_16x16x32_bf16 v[52:55], v[206:209], v[166:169], v[52:55]
	v_mfma_f32_16x16x32_bf16 v[40:43], v[198:201], v[174:177], v[40:43]
	v_mfma_f32_16x16x32_bf16 v[36:39], v[206:209], v[174:177], v[36:39]
	v_mfma_f32_16x16x32_bf16 v[24:27], v[198:201], v[182:185], v[24:27]
	v_mfma_f32_16x16x32_bf16 v[20:23], v[206:209], v[182:185], v[20:23]
	v_mfma_f32_16x16x32_bf16 v[8:11], v[198:201], v[190:193], v[8:11]
	v_mfma_f32_16x16x32_bf16 v[4:7], v[206:209], v[190:193], v[4:7]
	v_mfma_f32_16x16x32_bf16 v[56:59], v[202:205], v[170:173], v[56:59]
	v_mfma_f32_16x16x32_bf16 v[52:55], v[210:213], v[170:173], v[52:55]
	v_mfma_f32_16x16x32_bf16 v[40:43], v[202:205], v[178:181], v[40:43]
	v_mfma_f32_16x16x32_bf16 v[36:39], v[210:213], v[178:181], v[36:39]
	v_mfma_f32_16x16x32_bf16 v[24:27], v[202:205], v[186:189], v[24:27]
	v_mfma_f32_16x16x32_bf16 v[20:23], v[210:213], v[186:189], v[20:23]
	s_barrier
	v_mfma_f32_16x16x32_bf16 v[8:11], v[202:205], v[194:197], v[8:11]
	v_mfma_f32_16x16x32_bf16 v[4:7], v[210:213], v[194:197], v[4:7]
	s_setprio 0
	s_add_i32 s64, s64, 2
	s_add_u32 s34, s34, 0x100
	s_addc_u32 s35, s35, 0
	s_add_u32 s62, s62, 0x100
	s_addc_u32 s63, s63, 0
	s_cmp_gt_u32 s64, 13
	s_cbranch_scc1 .LBB0_1981
